# stack11 with unreachable padding so the downstream K-loops keep stack10 code alignment (isolates the mid-hook / preheader / scan edits from placement effects)
# speedup vs baseline: 1.0005x; 1.0005x over previous
; #define PG8_LDA(dst, b, h) do { _Pragma("unroll") for (int m = 0; m < 4; ++m) _Pragma("unroll") for (int k = 0; k < 2; ++k) dst[m][k] = *(const PG8_LAS bf16x8*)(lds + PG8_SA(b, h) + aoff + m * 2048 + k * 1024); } while (0)
; template <class Epi, class Sched, bool ALIGN_EPI = false, bool SP2 = false>
; __device__ __forceinline__ void gemm_phase(PG8_LAS unsigned char* lds, const Gemm g, const Sched& S, const Epi& E, Stopwatch& sw) {
;     ...
;         for (int t = 0; t < nt; t += 2) {
;             if constexpr (Epi::MID) { if (t == Epi::MID_T0 || t == Epi::MID_T1) E.mid(acc, cur, t, wr, wc, fr, fq); }
;             const bool last = (t == nt - 2);
;             const char* a1 = cA + (size_t)(t + 1) * kstep;
;             const char* a2 = last ? nA : cA + (size_t)(t + 2) * kstep; const char* b2 = last ? nB : cB + (size_t)(t + 2) * kstep;
;             const char* a3 = a2 + kstep; const char* b3 = b2 + kstep;
;             if (last && has_next) S.a_ready(nxt);
;             if constexpr (SP2) {
;             int relax = __builtin_amdgcn_readfirstlane((int)((ui > 0) && (t == 0))); asm volatile("" : "+s"(relax));
;             PG8_LDB(B0, 0, 0); PG8_LDB(B1, 0, 1); PG8_SCHED; PG8_LDA(At, 0, 0); if (!relax) PG8_STAGE(PG8_SA(1, 1), a1 + hstep, voffA);
;             if (relax) PG8_WAIT_VN(8 + Epi::NST); else PG8_WAIT_V(8); PG8_WAIT_L(0); PG8_BAR; PG8_MMA(0, 0, At, B0); PG8_MMA(0, 1, At, B1); PG8_BAR; PG8_SCHED;
;             PG8_LDA(At, 0, 1); PG8_STAGE(PG8_SB(0, 0), b2, voffB); PG8_STAGE(PG8_SB(0, 1), b2 + hstep, voffB); PG8_STAGE(PG8_SA(0, 0), a2, voffA);
;             if (relax) PG8_WAIT_VN(8 + Epi::NST); else PG8_WAIT_V(8); PG8_WAIT_L(0); PG8_BAR; PG8_MMA(1, 0, At, B0); PG8_MMA(1, 1, At, B1); PG8_BAR; PG8_SCHED;
;             PG8_LDB(B0, 1, 0); PG8_LDB(B1, 1, 1); PG8_SCHED; PG8_LDA(At, 1, 0); PG8_STAGE(PG8_SA(0, 1), a2 + hstep, voffA);
;             if (relax) PG8_WAIT_VN(8 + Epi::NST); else PG8_WAIT_V(8); PG8_WAIT_L(0); PG8_BAR; PG8_MMA(0, 0, At, B0); PG8_MMA(0, 1, At, B1); PG8_BAR; PG8_SCHED;
;             PG8_LDA(At, 1, 1); PG8_STAGE(PG8_SB(1, 0), b3, voffB); PG8_STAGE(PG8_SB(1, 1), b3 + hstep, voffB); PG8_STAGE(PG8_SA(1, 0), a3, voffA);
;             PG8_WAIT_V(8); PG8_WAIT_L(0); PG8_BAR; PG8_MMA(1, 0, At, B0); PG8_MMA(1, 1, At, B1); PG8_BAR; PG8_SCHED;
;             if (last && has_next) PG8_STAGE(PG8_SA(1, 1), a3 + hstep, voffA);
.LBB0_793:
	s_branch .LBB0_785
	s_nop 0
	s_nop 0
	s_nop 0

; __device__ __forceinline__ void xcd_barrier(const XcdBarrier& b) {
;     asm volatile("s_waitcnt vmcnt(0)" ::: "memory");
;     __syncthreads();
;     if (threadIdx.x == 0) {
;         unsigned* bar = b.bar;
;         __builtin_amdgcn_s_waitcnt(0);
;         unsigned nloc = b.st[0], nx = b.st[1];
;         if (nloc == 0u) { xcd_barrier_complete(bar, b.x, nloc, nx); b.st[0] = nloc; b.st[1] = nx; }
.LBB0_1029:
	v_readlane_b32 s0, v255, 27
	s_add_i32 s0, s0, 8
	s_cmp_ge_i32 s0, s87
	s_cbranch_scc1 .LBB0_1103
	v_readlane_b32 s4, v250, 50
	v_readlane_b32 s5, v250, 51
	s_mov_b64 s[38:39], -1
	s_and_b64 vcc, exec, s[4:5]
	s_cbranch_vccz .LBB0_1084
	s_waitcnt vmcnt(0)
	s_waitcnt vmcnt(0)
	s_barrier
	s_and_saveexec_b64 s[38:39], s[90:91]
	s_cbranch_execz .LBB0_1083
	v_readlane_b32 s3, v255, 3
	s_waitcnt vmcnt(0) expcnt(0) lgkmcnt(0)
	s_nop 0
	v_mov_b32_e32 v1, s3
	ds_read_b32 v4, v1
	v_readlane_b32 s3, v255, 4
	s_waitcnt lgkmcnt(0)
	v_cmp_ne_u32_e32 vcc, 0, v4
	v_mov_b32_e32 v1, s3
	ds_read_b32 v2, v1
	s_cbranch_vccnz .LBB0_1047
	v_readlane_b32 s18, v250, 0
	v_readlane_b32 s19, v250, 1
	s_load_dwordx2 s[4:5], s[18:19], 0x4
	s_waitcnt lgkmcnt(0)
	s_mul_i32 s3, s4, s88
	s_mul_i32 s3, s3, s5
	s_mov_b32 s4, 1
	s_branch .LBB0_1035
	s_nop 0
	s_nop 0
